# HGRN carry scan: 16 chunks' PC/SC loads requested together (4 batches of 32 loads, counted waits) instead of 64 dependent load-fma-store round trips
# speedup vs baseline: 1.0203x; 1.0109x over previous
.LBB0_477:
	v_lshl_add_u64 v[6:7], s[74:75], 0, v[4:5]
	v_lshl_add_u64 v[8:9], s[74:75], 0, v[2:3]
	s_mov_b64 s[14:15], 0x27851000
	v_lshl_add_u64 v[8:9], v[8:9], 0, s[14:15]
	s_mov_b64 s[14:15], 0x26851000
	v_lshl_add_u64 v[16:17], v[6:7], 0, s[14:15]
	s_mov_b64 s[14:15], 0x27891000
	v_lshl_add_u64 v[10:11], v[6:7], 0, s[14:15]
	s_mov_b64 s[14:15], 0x4000
	global_load_dword v212, v[8:9], off
	global_load_dword v213, v[8:9], off offset:256
	global_load_dword v214, v[8:9], off offset:512
	global_load_dword v215, v[8:9], off offset:768
	global_load_dword v216, v[8:9], off offset:1024
	global_load_dword v217, v[8:9], off offset:1280
	global_load_dword v218, v[8:9], off offset:1536
	global_load_dword v219, v[8:9], off offset:1792
	global_load_dword v220, v[8:9], off offset:2048
	global_load_dword v221, v[8:9], off offset:2304
	global_load_dword v222, v[8:9], off offset:2560
	global_load_dword v223, v[8:9], off offset:2816
	global_load_dword v234, v[8:9], off offset:3072
	global_load_dword v235, v[8:9], off offset:3328
	global_load_dword v236, v[8:9], off offset:3584
	global_load_dword v237, v[8:9], off offset:3840
	global_load_dword v238, v[16:17], off
	v_lshl_add_u64 v[16:17], v[16:17], 0, s[14:15]
	global_load_dword v239, v[16:17], off
	v_lshl_add_u64 v[16:17], v[16:17], 0, s[14:15]
	global_load_dword v240, v[16:17], off
	v_lshl_add_u64 v[16:17], v[16:17], 0, s[14:15]
	global_load_dword v241, v[16:17], off
	v_lshl_add_u64 v[16:17], v[16:17], 0, s[14:15]
	global_load_dword v242, v[16:17], off
	v_lshl_add_u64 v[16:17], v[16:17], 0, s[14:15]
	global_load_dword v243, v[16:17], off
	v_lshl_add_u64 v[16:17], v[16:17], 0, s[14:15]
	global_load_dword v244, v[16:17], off
	v_lshl_add_u64 v[16:17], v[16:17], 0, s[14:15]
	global_load_dword v245, v[16:17], off
	v_lshl_add_u64 v[16:17], v[16:17], 0, s[14:15]
	global_load_dword v246, v[16:17], off
	v_lshl_add_u64 v[16:17], v[16:17], 0, s[14:15]
	global_load_dword v247, v[16:17], off
	v_lshl_add_u64 v[16:17], v[16:17], 0, s[14:15]
	global_load_dword v248, v[16:17], off
	v_lshl_add_u64 v[16:17], v[16:17], 0, s[14:15]
	global_load_dword v249, v[16:17], off
	v_lshl_add_u64 v[16:17], v[16:17], 0, s[14:15]
	global_load_dword v227, v[16:17], off
	v_lshl_add_u64 v[16:17], v[16:17], 0, s[14:15]
	global_load_dword v229, v[16:17], off
	v_lshl_add_u64 v[16:17], v[16:17], 0, s[14:15]
	global_load_dword v230, v[16:17], off
	v_lshl_add_u64 v[16:17], v[16:17], 0, s[14:15]
	global_load_dword v231, v[16:17], off
	global_store_dword v[10:11], v14, off
	v_lshl_add_u64 v[10:11], v[10:11], 0, s[14:15]
	s_waitcnt vmcnt(16)
	v_fmac_f32_e32 v238, v14, v212
	global_store_dword v[10:11], v238, off
	v_lshl_add_u64 v[10:11], v[10:11], 0, s[14:15]
	s_waitcnt vmcnt(16)
	v_fmac_f32_e32 v239, v238, v213
	global_store_dword v[10:11], v239, off
	v_lshl_add_u64 v[10:11], v[10:11], 0, s[14:15]
	s_waitcnt vmcnt(16)
	v_fmac_f32_e32 v240, v239, v214
	global_store_dword v[10:11], v240, off
	v_lshl_add_u64 v[10:11], v[10:11], 0, s[14:15]
	s_waitcnt vmcnt(16)
	v_fmac_f32_e32 v241, v240, v215
	global_store_dword v[10:11], v241, off
	v_lshl_add_u64 v[10:11], v[10:11], 0, s[14:15]
	s_waitcnt vmcnt(16)
	v_fmac_f32_e32 v242, v241, v216
	global_store_dword v[10:11], v242, off
	v_lshl_add_u64 v[10:11], v[10:11], 0, s[14:15]
	s_waitcnt vmcnt(16)
	v_fmac_f32_e32 v243, v242, v217
	global_store_dword v[10:11], v243, off
	v_lshl_add_u64 v[10:11], v[10:11], 0, s[14:15]
	s_waitcnt vmcnt(16)
	v_fmac_f32_e32 v244, v243, v218
	global_store_dword v[10:11], v244, off
	v_lshl_add_u64 v[10:11], v[10:11], 0, s[14:15]
	s_waitcnt vmcnt(16)
	v_fmac_f32_e32 v245, v244, v219
	global_store_dword v[10:11], v245, off
	v_lshl_add_u64 v[10:11], v[10:11], 0, s[14:15]
	s_waitcnt vmcnt(16)
	v_fmac_f32_e32 v246, v245, v220
	global_store_dword v[10:11], v246, off
	v_lshl_add_u64 v[10:11], v[10:11], 0, s[14:15]
	s_waitcnt vmcnt(16)
	v_fmac_f32_e32 v247, v246, v221
	global_store_dword v[10:11], v247, off
	v_lshl_add_u64 v[10:11], v[10:11], 0, s[14:15]
	s_waitcnt vmcnt(16)
	v_fmac_f32_e32 v248, v247, v222
	global_store_dword v[10:11], v248, off
	v_lshl_add_u64 v[10:11], v[10:11], 0, s[14:15]
	s_waitcnt vmcnt(16)
	v_fmac_f32_e32 v249, v248, v223
	global_store_dword v[10:11], v249, off
	v_lshl_add_u64 v[10:11], v[10:11], 0, s[14:15]
	s_waitcnt vmcnt(16)
	v_fmac_f32_e32 v227, v249, v234
	global_store_dword v[10:11], v227, off
	v_lshl_add_u64 v[10:11], v[10:11], 0, s[14:15]
	s_waitcnt vmcnt(16)
	v_fmac_f32_e32 v229, v227, v235
	global_store_dword v[10:11], v229, off
	v_lshl_add_u64 v[10:11], v[10:11], 0, s[14:15]
	s_waitcnt vmcnt(16)
	v_fmac_f32_e32 v230, v229, v236
	global_store_dword v[10:11], v230, off
	s_waitcnt vmcnt(16)
	v_fmac_f32_e32 v231, v230, v237
	v_mov_b32_e32 v14, v231
	s_mov_b64 s[14:15], 0x1000
	v_lshl_add_u64 v[2:3], v[2:3], 0, s[14:15]
	s_mov_b64 s[14:15], 0x40000
	v_lshl_add_u64 v[4:5], v[4:5], 0, s[14:15]
	s_sub_i32 s2, s2, 16
	s_cmp_eq_u32 s2, 0
	s_cbranch_scc0 .LBB0_477
	v_readlane_b32 s2, v254, 9
	s_mov_b32 s14, s2
	v_add_u32_e32 v12, s14, v12
	s_mov_b32 s2, 0xffff
	v_cmp_lt_i32_e32 vcc, s2, v12
	s_or_b64 s[12:13], vcc, s[12:13]
	v_add_u16_e32 v13, s14, v13
	v_readlane_b32 s3, v254, 10
	s_andn2_b64 exec, exec, s[12:13]
	s_cbranch_execnz .LBB0_476
